# P6a (EpiMA) epilogue: gate rows of the later groups touched right after the first group's loads (L2 prefetch); on top of v6
# speedup vs baseline: 1.0065x; 1.0065x over previous
.LBB0_1025:
	ds_read_b128 v[0:3], v186
	ds_read_b128 v[4:7], v190
	ds_read_b128 v[8:11], v191
	ds_read_b128 v[12:15], v192
	s_add_u32 s34, s30, 0x80
	s_addc_u32 s35, s31, 0
	s_cmp_eq_u32 s65, 12
	s_cselect_b32 s37, s21, s35
	s_cselect_b32 s36, s61, s34
	s_cselect_b32 s35, s23, s64
	s_cselect_b32 s34, s62, s63
	v_lshl_add_u64 v[160:161], s[30:31], 0, v[158:159]
	s_add_i32 m0, s29, 0xc000
	ds_read_b128 v[206:209], v203
	ds_read_b128 v[210:213], v203 offset:1024
	ds_read_b128 v[214:217], v203 offset:2048
	ds_read_b128 v[218:221], v203 offset:3072
	ds_read_b128 v[222:225], v203 offset:4096
	ds_read_b128 v[226:229], v203 offset:5120
	ds_read_b128 v[230:233], v203 offset:6144
	ds_read_b128 v[234:237], v203 offset:7168
	global_load_lds_dwordx4 v[160:161], off
	v_lshl_add_u64 v[160:161], s[30:31], 0, v[156:157]
	s_add_i32 m0, s29, 0xe000
	s_nop 0
	global_load_lds_dwordx4 v[160:161], off
	s_waitcnt lgkmcnt(8)
	s_barrier
	s_waitcnt lgkmcnt(0)
	s_setprio 1
	s_waitcnt lgkmcnt(0)
	v_mfma_scale_f32_16x16x128_f8f6f4 v[140:143], v[0:7], v[206:213], v[140:143], v204, v205 op_sel_hi:[0,0,0]
	v_mfma_scale_f32_16x16x128_f8f6f4 v[136:139], v[8:15], v[206:213], v[136:139], v204, v205 op_sel_hi:[0,0,0]
	v_mfma_scale_f32_16x16x128_f8f6f4 v[132:135], v[0:7], v[214:221], v[132:135], v204, v205 op_sel_hi:[0,0,0]
	v_mfma_scale_f32_16x16x128_f8f6f4 v[128:131], v[8:15], v[214:221], v[128:131], v204, v205 op_sel_hi:[0,0,0]
	v_mfma_scale_f32_16x16x128_f8f6f4 v[124:127], v[0:7], v[222:229], v[124:127], v204, v205 op_sel_hi:[0,0,0]
	v_mfma_scale_f32_16x16x128_f8f6f4 v[120:123], v[8:15], v[222:229], v[120:123], v204, v205 op_sel_hi:[0,0,0]
	v_mfma_scale_f32_16x16x128_f8f6f4 v[116:119], v[0:7], v[230:237], v[116:119], v204, v205 op_sel_hi:[0,0,0]
	v_mfma_scale_f32_16x16x128_f8f6f4 v[112:115], v[8:15], v[230:237], v[112:115], v204, v205 op_sel_hi:[0,0,0]
	s_setprio 0
	s_barrier
	s_mov_b32 m0, s45
	v_lshl_add_u64 v[160:161], s[34:35], 0, v[144:145]
	ds_read_b128 v[238:241], v187
	ds_read_b128 v[242:245], v193
	ds_read_b128 v[246:249], v194
	ds_read_b128 v[250:253], v195
	global_load_lds_dwordx4 v[160:161], off
	v_lshl_add_u64 v[162:163], s[34:35], 0, v[146:147]
	s_mov_b32 m0, s46
	s_nop 0
	global_load_lds_dwordx4 v[162:163], off
	s_barrier
	s_waitcnt lgkmcnt(0)
	s_setprio 1
	s_waitcnt lgkmcnt(0)
	v_mfma_scale_f32_16x16x128_f8f6f4 v[108:111], v[238:245], v[206:213], v[108:111], v204, v205 op_sel_hi:[0,0,0]
	v_mfma_scale_f32_16x16x128_f8f6f4 v[104:107], v[246:253], v[206:213], v[104:107], v204, v205 op_sel_hi:[0,0,0]
	v_mfma_scale_f32_16x16x128_f8f6f4 v[100:103], v[238:245], v[214:221], v[100:103], v204, v205 op_sel_hi:[0,0,0]
	v_mfma_scale_f32_16x16x128_f8f6f4 v[96:99], v[246:253], v[214:221], v[96:99], v204, v205 op_sel_hi:[0,0,0]
	v_mfma_scale_f32_16x16x128_f8f6f4 v[92:95], v[238:245], v[222:229], v[92:95], v204, v205 op_sel_hi:[0,0,0]
	v_mfma_scale_f32_16x16x128_f8f6f4 v[88:91], v[246:253], v[222:229], v[88:91], v204, v205 op_sel_hi:[0,0,0]
	v_mfma_scale_f32_16x16x128_f8f6f4 v[84:87], v[238:245], v[230:237], v[84:87], v204, v205 op_sel_hi:[0,0,0]
	v_mfma_scale_f32_16x16x128_f8f6f4 v[80:83], v[246:253], v[230:237], v[80:83], v204, v205 op_sel_hi:[0,0,0]
	s_setprio 0
	s_mov_b32 m0, s29
	v_lshl_add_u64 v[164:165], s[36:37], 0, v[148:149]
	s_barrier
	ds_read_b128 v[206:209], v203 offset:16384
	ds_read_b128 v[210:213], v203 offset:17408
	ds_read_b128 v[214:217], v203 offset:18432
	ds_read_b128 v[218:221], v203 offset:19456
	ds_read_b128 v[222:225], v203 offset:20480
	ds_read_b128 v[226:229], v203 offset:21504
	ds_read_b128 v[230:233], v203 offset:22528
	ds_read_b128 v[234:237], v203 offset:23552
	global_load_lds_dwordx4 v[164:165], off
	v_lshl_add_u64 v[166:167], s[36:37], 0, v[150:151]
	s_mov_b32 m0, s47
	s_nop 0
	global_load_lds_dwordx4 v[166:167], off
	s_barrier
	s_waitcnt lgkmcnt(0)
	s_setprio 1
	s_waitcnt lgkmcnt(0)
	v_mfma_scale_f32_16x16x128_f8f6f4 v[76:79], v[0:7], v[206:213], v[76:79], v204, v205 op_sel_hi:[0,0,0]
	v_mfma_scale_f32_16x16x128_f8f6f4 v[72:75], v[8:15], v[206:213], v[72:75], v204, v205 op_sel_hi:[0,0,0]
	v_mfma_scale_f32_16x16x128_f8f6f4 v[68:71], v[0:7], v[214:221], v[68:71], v204, v205 op_sel_hi:[0,0,0]
	v_mfma_scale_f32_16x16x128_f8f6f4 v[64:67], v[8:15], v[214:221], v[64:67], v204, v205 op_sel_hi:[0,0,0]
	v_mfma_scale_f32_16x16x128_f8f6f4 v[60:63], v[0:7], v[222:229], v[60:63], v204, v205 op_sel_hi:[0,0,0]
	v_mfma_scale_f32_16x16x128_f8f6f4 v[56:59], v[8:15], v[222:229], v[56:59], v204, v205 op_sel_hi:[0,0,0]
	v_mfma_scale_f32_16x16x128_f8f6f4 v[52:55], v[0:7], v[230:237], v[52:55], v204, v205 op_sel_hi:[0,0,0]
	v_mfma_scale_f32_16x16x128_f8f6f4 v[48:51], v[8:15], v[230:237], v[48:51], v204, v205 op_sel_hi:[0,0,0]
	s_setprio 0
	s_barrier
	s_add_u32 s66, s34, 0x40000
	s_addc_u32 s67, s35, 0
	s_mov_b32 m0, s48
	v_lshl_add_u64 v[0:1], s[66:67], 0, v[144:145]
	global_load_lds_dwordx4 v[0:1], off
	v_lshl_add_u64 v[0:1], s[66:67], 0, v[146:147]
	s_mov_b32 m0, s49
	s_nop 0
	global_load_lds_dwordx4 v[0:1], off
	s_waitcnt vmcnt(6)
	s_barrier
	s_setprio 1
	v_mfma_scale_f32_16x16x128_f8f6f4 v[44:47], v[238:245], v[206:213], v[44:47], v204, v205 op_sel_hi:[0,0,0]
	v_mfma_scale_f32_16x16x128_f8f6f4 v[40:43], v[246:253], v[206:213], v[40:43], v204, v205 op_sel_hi:[0,0,0]
	v_mfma_scale_f32_16x16x128_f8f6f4 v[36:39], v[238:245], v[214:221], v[36:39], v204, v205 op_sel_hi:[0,0,0]
	v_mfma_scale_f32_16x16x128_f8f6f4 v[32:35], v[246:253], v[214:221], v[32:35], v204, v205 op_sel_hi:[0,0,0]
	v_mfma_scale_f32_16x16x128_f8f6f4 v[28:31], v[238:245], v[222:229], v[28:31], v204, v205 op_sel_hi:[0,0,0]
	v_mfma_scale_f32_16x16x128_f8f6f4 v[24:27], v[246:253], v[222:229], v[24:27], v204, v205 op_sel_hi:[0,0,0]
	v_mfma_scale_f32_16x16x128_f8f6f4 v[20:23], v[238:245], v[230:237], v[20:23], v204, v205 op_sel_hi:[0,0,0]
	v_mfma_scale_f32_16x16x128_f8f6f4 v[16:19], v[246:253], v[230:237], v[16:19], v204, v205 op_sel_hi:[0,0,0]
	s_setprio 0
	s_barrier
	ds_read_b128 v[0:3], v188
	ds_read_b128 v[4:7], v196
	ds_read_b128 v[8:11], v197
	ds_read_b128 v[12:15], v198
	s_mov_b32 m0, s50
	v_lshl_add_u64 v[168:169], s[36:37], 0, v[152:153]
	ds_read_b128 v[206:209], v203 offset:32768
	ds_read_b128 v[210:213], v203 offset:33792
	ds_read_b128 v[214:217], v203 offset:34816
	ds_read_b128 v[218:221], v203 offset:35840
	ds_read_b128 v[222:225], v203 offset:36864
	ds_read_b128 v[226:229], v203 offset:37888
	ds_read_b128 v[230:233], v203 offset:38912
	ds_read_b128 v[234:237], v203 offset:39936
	global_load_lds_dwordx4 v[168:169], off
	v_lshl_add_u64 v[168:169], s[36:37], 0, v[154:155]
	s_mov_b32 m0, s51
	s_nop 0
	global_load_lds_dwordx4 v[168:169], off
	s_waitcnt lgkmcnt(8)
	s_barrier
	s_waitcnt lgkmcnt(0)
	s_setprio 1
	s_waitcnt lgkmcnt(0)
	v_mfma_scale_f32_16x16x128_f8f6f4 v[140:143], v[0:7], v[206:213], v[140:143], v204, v205 op_sel_hi:[0,0,0]
	v_mfma_scale_f32_16x16x128_f8f6f4 v[136:139], v[8:15], v[206:213], v[136:139], v204, v205 op_sel_hi:[0,0,0]
	v_mfma_scale_f32_16x16x128_f8f6f4 v[132:135], v[0:7], v[214:221], v[132:135], v204, v205 op_sel_hi:[0,0,0]
	v_mfma_scale_f32_16x16x128_f8f6f4 v[128:131], v[8:15], v[214:221], v[128:131], v204, v205 op_sel_hi:[0,0,0]
	v_mfma_scale_f32_16x16x128_f8f6f4 v[124:127], v[0:7], v[222:229], v[124:127], v204, v205 op_sel_hi:[0,0,0]
	v_mfma_scale_f32_16x16x128_f8f6f4 v[120:123], v[8:15], v[222:229], v[120:123], v204, v205 op_sel_hi:[0,0,0]
	v_mfma_scale_f32_16x16x128_f8f6f4 v[116:119], v[0:7], v[230:237], v[116:119], v204, v205 op_sel_hi:[0,0,0]
	v_mfma_scale_f32_16x16x128_f8f6f4 v[112:115], v[8:15], v[230:237], v[112:115], v204, v205 op_sel_hi:[0,0,0]
	s_setprio 0
	s_barrier
	s_mov_b32 m0, s53
	v_lshl_add_u64 v[160:161], v[160:161], 0, s[0:1]
	ds_read_b128 v[238:241], v189
	ds_read_b128 v[242:245], v199
	ds_read_b128 v[246:249], v200
	ds_read_b128 v[250:253], v201
	global_load_lds_dwordx4 v[160:161], off
	v_lshl_add_u64 v[160:161], v[162:163], 0, s[0:1]
	s_mov_b32 m0, s54
	s_nop 0
	global_load_lds_dwordx4 v[160:161], off
	s_barrier
	s_waitcnt lgkmcnt(0)
	s_setprio 1
	s_waitcnt lgkmcnt(0)
	v_mfma_scale_f32_16x16x128_f8f6f4 v[108:111], v[238:245], v[206:213], v[108:111], v204, v205 op_sel_hi:[0,0,0]
	v_mfma_scale_f32_16x16x128_f8f6f4 v[104:107], v[246:253], v[206:213], v[104:107], v204, v205 op_sel_hi:[0,0,0]
	v_mfma_scale_f32_16x16x128_f8f6f4 v[100:103], v[238:245], v[214:221], v[100:103], v204, v205 op_sel_hi:[0,0,0]
	v_mfma_scale_f32_16x16x128_f8f6f4 v[96:99], v[246:253], v[214:221], v[96:99], v204, v205 op_sel_hi:[0,0,0]
	v_mfma_scale_f32_16x16x128_f8f6f4 v[92:95], v[238:245], v[222:229], v[92:95], v204, v205 op_sel_hi:[0,0,0]
	v_mfma_scale_f32_16x16x128_f8f6f4 v[88:91], v[246:253], v[222:229], v[88:91], v204, v205 op_sel_hi:[0,0,0]
	v_mfma_scale_f32_16x16x128_f8f6f4 v[84:87], v[238:245], v[230:237], v[84:87], v204, v205 op_sel_hi:[0,0,0]
	v_mfma_scale_f32_16x16x128_f8f6f4 v[80:83], v[246:253], v[230:237], v[80:83], v204, v205 op_sel_hi:[0,0,0]
	s_setprio 0
	s_mov_b32 m0, s55
	v_lshl_add_u64 v[160:161], v[164:165], 0, s[0:1]
	s_barrier
	ds_read_b128 v[206:209], v203 offset:49152
	ds_read_b128 v[210:213], v203 offset:50176
	ds_read_b128 v[214:217], v203 offset:51200
	ds_read_b128 v[218:221], v203 offset:52224
	ds_read_b128 v[222:225], v203 offset:53248
	ds_read_b128 v[226:229], v203 offset:54272
	ds_read_b128 v[230:233], v203 offset:55296
	ds_read_b128 v[234:237], v203 offset:56320
	global_load_lds_dwordx4 v[160:161], off
	v_lshl_add_u64 v[160:161], v[166:167], 0, s[0:1]
	s_mov_b32 m0, s56
	s_nop 0
	global_load_lds_dwordx4 v[160:161], off
	s_barrier
	s_waitcnt lgkmcnt(0)
	s_setprio 1
	s_waitcnt lgkmcnt(0)
	v_mfma_scale_f32_16x16x128_f8f6f4 v[76:79], v[0:7], v[206:213], v[76:79], v204, v205 op_sel_hi:[0,0,0]
	v_mfma_scale_f32_16x16x128_f8f6f4 v[72:75], v[8:15], v[206:213], v[72:75], v204, v205 op_sel_hi:[0,0,0]
	v_mfma_scale_f32_16x16x128_f8f6f4 v[68:71], v[0:7], v[214:221], v[68:71], v204, v205 op_sel_hi:[0,0,0]
	v_mfma_scale_f32_16x16x128_f8f6f4 v[64:67], v[8:15], v[214:221], v[64:67], v204, v205 op_sel_hi:[0,0,0]
	v_mfma_scale_f32_16x16x128_f8f6f4 v[60:63], v[0:7], v[222:229], v[60:63], v204, v205 op_sel_hi:[0,0,0]
	v_mfma_scale_f32_16x16x128_f8f6f4 v[56:59], v[8:15], v[222:229], v[56:59], v204, v205 op_sel_hi:[0,0,0]
	v_mfma_scale_f32_16x16x128_f8f6f4 v[52:55], v[0:7], v[230:237], v[52:55], v204, v205 op_sel_hi:[0,0,0]
	v_mfma_scale_f32_16x16x128_f8f6f4 v[48:51], v[8:15], v[230:237], v[48:51], v204, v205 op_sel_hi:[0,0,0]
	s_setprio 0
	s_barrier
	s_add_u32 s34, s34, 0x40080
	s_addc_u32 s35, s35, 0
	s_mov_b32 m0, s57
	v_lshl_add_u64 v[0:1], s[34:35], 0, v[144:145]
	global_load_lds_dwordx4 v[0:1], off
	v_lshl_add_u64 v[0:1], s[34:35], 0, v[146:147]
	s_mov_b32 m0, s58
	s_nop 0
	global_load_lds_dwordx4 v[0:1], off
	s_waitcnt vmcnt(6)
	s_barrier
	s_setprio 1
	v_mfma_scale_f32_16x16x128_f8f6f4 v[44:47], v[238:245], v[206:213], v[44:47], v204, v205 op_sel_hi:[0,0,0]
	v_mfma_scale_f32_16x16x128_f8f6f4 v[40:43], v[246:253], v[206:213], v[40:43], v204, v205 op_sel_hi:[0,0,0]
	v_mfma_scale_f32_16x16x128_f8f6f4 v[36:39], v[238:245], v[214:221], v[36:39], v204, v205 op_sel_hi:[0,0,0]
	v_mfma_scale_f32_16x16x128_f8f6f4 v[32:35], v[246:253], v[214:221], v[32:35], v204, v205 op_sel_hi:[0,0,0]
	v_mfma_scale_f32_16x16x128_f8f6f4 v[28:31], v[238:245], v[222:229], v[28:31], v204, v205 op_sel_hi:[0,0,0]
	v_mfma_scale_f32_16x16x128_f8f6f4 v[24:27], v[246:253], v[222:229], v[24:27], v204, v205 op_sel_hi:[0,0,0]
	v_mfma_scale_f32_16x16x128_f8f6f4 v[20:23], v[238:245], v[230:237], v[20:23], v204, v205 op_sel_hi:[0,0,0]
	v_mfma_scale_f32_16x16x128_f8f6f4 v[16:19], v[246:253], v[230:237], v[16:19], v204, v205 op_sel_hi:[0,0,0]
	s_setprio 0
	s_add_i32 s65, s65, 2
	s_add_u32 s30, s30, 0x100
	s_addc_u32 s31, s31, 0
	s_add_u32 s63, s63, 0x100
	s_addc_u32 s64, s64, 0
	s_cmp_gt_u32 s65, 13
	s_barrier
	s_cbranch_scc0 .LBB0_1025
	v_lshl_add_u32 v6, s28, 8, v185
	v_lshl_or_b32 v10, s60, 8, v202
	v_mov_b64_e32 v[8:9], s[8:9]
	v_ashrrev_i32_e32 v11, 31, v10
	v_mad_i64_i32 v[0:1], s[30:31], v6, s59, v[8:9]
	v_lshl_add_u64 v[12:13], v[0:1], 0, s[16:17]
	v_lshlrev_b64 v[4:5], 1, v[10:11]
	s_nop 15
	s_nop 15
	v_lshl_add_u64 v[0:1], v[12:13], 0, v[4:5]
	global_load_dwordx4 v[206:209], v[0:1], off
	v_or_b32_e32 v218, 16, v6
	v_mad_i64_i32 v[0:1], s[30:31], v218, s59, v[8:9]
	v_lshl_add_u64 v[14:15], v[0:1], 0, s[16:17]
	v_lshl_add_u64 v[0:1], v[14:15], 0, v[4:5]
	global_load_dwordx4 v[210:213], v[0:1], off
	v_or_b32_e32 v168, 32, v6
	v_ashrrev_i32_e32 v7, 31, v6
	v_or_b32_e32 v162, 48, v6
	v_mad_i64_i32 v[0:1], s[30:31], v168, s59, v[8:9]
	v_mad_i64_i32 v[2:3], s[30:31], v162, s59, v[8:9]
	v_lshlrev_b64 v[160:161], 12, v[6:7]
	v_lshl_add_u64 v[166:167], v[0:1], 0, s[16:17]
	v_lshl_add_u64 v[164:165], v[2:3], 0, s[16:17]
	v_lshl_add_u64 v[0:1], s[6:7], 0, v[160:161]
	v_lshl_add_u64 v[2:3], v[166:167], 0, v[4:5]
	v_lshl_add_u64 v[220:221], v[164:165], 0, v[4:5]
	v_lshl_add_u64 v[160:161], v[0:1], 0, v[4:5]
	global_load_dwordx4 v[214:217], v[2:3], off
	s_nop 0
	global_load_dwordx4 v[0:3], v[220:221], off
	v_add_u32_e32 v244, 0, v6
	v_mad_i64_i32 v[246:247], s[30:31], v244, s59, v[8:9]
	v_lshl_add_u64 v[246:247], v[246:247], 0, s[16:17]
	v_lshl_add_u64 v[246:247], v[246:247], 0, v[4:5]
	global_load_dword v250, v[246:247], off offset:256
	v_add_u32_e32 v244, 16, v6
	v_mad_i64_i32 v[246:247], s[30:31], v244, s59, v[8:9]
	v_lshl_add_u64 v[246:247], v[246:247], 0, s[16:17]
	v_lshl_add_u64 v[246:247], v[246:247], 0, v[4:5]
	global_load_dword v250, v[246:247], off offset:256
	v_add_u32_e32 v244, 32, v6
	v_mad_i64_i32 v[246:247], s[30:31], v244, s59, v[8:9]
	v_lshl_add_u64 v[246:247], v[246:247], 0, s[16:17]
	v_lshl_add_u64 v[246:247], v[246:247], 0, v[4:5]
	global_load_dword v250, v[246:247], off offset:256
	v_add_u32_e32 v244, 48, v6
	v_mad_i64_i32 v[246:247], s[30:31], v244, s59, v[8:9]
	v_lshl_add_u64 v[246:247], v[246:247], 0, s[16:17]
	v_lshl_add_u64 v[246:247], v[246:247], 0, v[4:5]
	global_load_dword v250, v[246:247], off offset:256
	v_add_u32_e32 v244, 128, v6
	v_mad_i64_i32 v[246:247], s[30:31], v244, s59, v[8:9]
	v_lshl_add_u64 v[246:247], v[246:247], 0, s[16:17]
	v_lshl_add_u64 v[246:247], v[246:247], 0, v[4:5]
	global_load_dword v250, v[246:247], off
	global_load_dword v250, v[246:247], off offset:256
	v_add_u32_e32 v244, 144, v6
	v_mad_i64_i32 v[246:247], s[30:31], v244, s59, v[8:9]
	v_lshl_add_u64 v[246:247], v[246:247], 0, s[16:17]
	v_lshl_add_u64 v[246:247], v[246:247], 0, v[4:5]
	global_load_dword v250, v[246:247], off
	global_load_dword v250, v[246:247], off offset:256
	v_add_u32_e32 v244, 160, v6
	v_mad_i64_i32 v[246:247], s[30:31], v244, s59, v[8:9]
	v_lshl_add_u64 v[246:247], v[246:247], 0, s[16:17]
	v_lshl_add_u64 v[246:247], v[246:247], 0, v[4:5]
	global_load_dword v250, v[246:247], off
	global_load_dword v250, v[246:247], off offset:256
	v_add_u32_e32 v244, 176, v6
	v_mad_i64_i32 v[246:247], s[30:31], v244, s59, v[8:9]
	v_lshl_add_u64 v[246:247], v[246:247], 0, s[16:17]
	v_lshl_add_u64 v[246:247], v[246:247], 0, v[4:5]
	global_load_dword v250, v[246:247], off
	global_load_dword v250, v[246:247], off offset:256
	v_ashrrev_i32_e32 v219, 31, v218
	v_ashrrev_i32_e32 v169, 31, v168
	v_ashrrev_i32_e32 v163, 31, v162
	s_and_b64 vcc, exec, s[18:19]
	s_mov_b32 s60, s22
	s_mov_b32 s28, s20
	s_mov_b64 s[34:35], s[26:27]
	s_waitcnt vmcnt(0)
	v_lshlrev_b32_e32 v7, 16, v206
	v_and_b32_e32 v11, 0xffff0000, v206
	v_lshlrev_b32_e32 v206, 16, v207
	v_and_b32_e32 v207, 0xffff0000, v207
	v_lshlrev_b32_e32 v220, 16, v208
	v_and_b32_e32 v208, 0xffff0000, v208
	v_lshlrev_b32_e32 v221, 16, v209
	v_and_b32_e32 v209, 0xffff0000, v209
	v_mul_f32_e32 v7, 0xbfb8aa3b, v7
	v_mul_f32_e32 v11, 0xbfb8aa3b, v11
	v_mul_f32_e32 v206, 0xbfb8aa3b, v206
	v_mul_f32_e32 v207, 0xbfb8aa3b, v207
	v_mul_f32_e32 v220, 0xbfb8aa3b, v220
	v_mul_f32_e32 v208, 0xbfb8aa3b, v208
	v_mul_f32_e32 v221, 0xbfb8aa3b, v221
	v_mul_f32_e32 v209, 0xbfb8aa3b, v209
	v_exp_f32_e32 v7, v7
	v_exp_f32_e32 v11, v11
	v_exp_f32_e32 v206, v206
	v_exp_f32_e32 v207, v207
	v_exp_f32_e32 v220, v220
	v_exp_f32_e32 v208, v208
	v_exp_f32_e32 v221, v221
	v_exp_f32_e32 v209, v209
	v_lshlrev_b32_e32 v222, 16, v210
	v_and_b32_e32 v210, 0xffff0000, v210
	v_lshlrev_b32_e32 v223, 16, v211
	v_mul_f32_e32 v222, 0xbfb8aa3b, v222
	v_mul_f32_e32 v210, 0xbfb8aa3b, v210
	v_mul_f32_e32 v223, 0xbfb8aa3b, v223
	v_exp_f32_e32 v224, v222
	v_exp_f32_e32 v210, v210
	v_exp_f32_e32 v226, v223
	v_add_f32_e32 v7, 1.0, v7
	v_add_f32_e32 v11, 1.0, v11
	v_add_f32_e32 v222, 1.0, v206
	v_add_f32_e32 v223, 1.0, v207
	v_add_f32_e32 v220, 1.0, v220
	v_add_f32_e32 v225, 1.0, v208
	v_add_f32_e32 v227, 1.0, v221
	v_add_f32_e32 v228, 1.0, v209
	v_rcp_f32_e32 v206, v7
	v_rcp_f32_e32 v207, v11
	v_rcp_f32_e32 v208, v222
	v_rcp_f32_e32 v209, v223
	v_rcp_f32_e32 v220, v220
	v_rcp_f32_e32 v221, v225
	v_rcp_f32_e32 v222, v227
	v_rcp_f32_e32 v223, v228
	v_add_f32_e32 v11, 1.0, v210
	v_rcp_f32_e32 v225, v11
	v_pk_mul_f32 v[140:141], v[140:141], v[206:207]
	v_pk_mul_f32 v[206:207], v[138:139], v[222:223]
	v_pk_mul_f32 v[138:139], v[136:137], v[220:221]
	v_cvt_pk_bf16_f32 v136, v140, v141
	v_and_b32_e32 v11, 0xffff0000, v211
	v_pk_mul_f32 v[142:143], v[142:143], v[208:209]
	v_mul_f32_e32 v11, 0xbfb8aa3b, v11
	v_cvt_pk_bf16_f32 v137, v142, v143
	v_cvt_pk_bf16_f32 v138, v138, v139
	v_cvt_pk_bf16_f32 v139, v206, v207
	global_store_dwordx4 v[160:161], v[136:139], off
	v_exp_f32_e32 v11, v11
	v_add_f32_e32 v7, 1.0, v224
	v_lshlrev_b32_e32 v136, 16, v212
	v_mul_f32_e32 v136, 0xbfb8aa3b, v136
	v_exp_f32_e32 v138, v136
	v_rcp_f32_e32 v224, v7
	v_add_f32_e32 v7, 1.0, v226
	v_rcp_f32_e32 v136, v7
	v_add_f32_e32 v7, 1.0, v11
	v_rcp_f32_e32 v137, v7
	v_add_f32_e32 v7, 1.0, v138
	v_rcp_f32_e32 v138, v7
	v_and_b32_e32 v7, 0xffff0000, v212
	v_lshlrev_b32_e32 v11, 16, v213
	v_mul_f32_e32 v7, 0xbfb8aa3b, v7
	v_mul_f32_e32 v11, 0xbfb8aa3b, v11
	v_and_b32_e32 v139, 0xffff0000, v213
	v_exp_f32_e32 v7, v7
	v_exp_f32_e32 v11, v11
	v_mul_f32_e32 v139, 0xbfb8aa3b, v139
	v_exp_f32_e32 v139, v139
	v_add_f32_e32 v7, 1.0, v7
	v_add_f32_e32 v11, 1.0, v11
	v_rcp_f32_e32 v140, v11
	v_add_f32_e32 v11, 1.0, v139
	v_rcp_f32_e32 v139, v7
	v_rcp_f32_e32 v141, v11
	v_pk_mul_f32 v[132:133], v[132:133], v[224:225]
	v_pk_mul_f32 v[134:135], v[134:135], v[136:137]
	v_pk_mul_f32 v[128:129], v[128:129], v[138:139]
	v_pk_mul_f32 v[136:137], v[130:131], v[140:141]
	v_cvt_pk_bf16_f32 v130, v132, v133
	v_cvt_pk_bf16_f32 v131, v134, v135
	v_cvt_pk_bf16_f32 v132, v128, v129
	v_lshlrev_b64 v[128:129], 12, v[218:219]
	v_lshlrev_b32_e32 v7, 16, v214
	v_lshl_add_u64 v[128:129], s[6:7], 0, v[128:129]
	v_mul_f32_e32 v7, 0xbfb8aa3b, v7
	v_lshl_add_u64 v[128:129], v[128:129], 0, v[4:5]
	v_and_b32_e32 v11, 0xffff0000, v214
	v_cvt_pk_bf16_f32 v133, v136, v137
	v_exp_f32_e32 v7, v7
	global_store_dwordx4 v[128:129], v[130:133], off
	v_mul_f32_e32 v11, 0xbfb8aa3b, v11
	v_exp_f32_e32 v11, v11
	v_lshlrev_b32_e32 v130, 16, v215
	v_mul_f32_e32 v130, 0xbfb8aa3b, v130
	v_exp_f32_e32 v132, v130
	v_add_f32_e32 v7, 1.0, v7
	v_rcp_f32_e32 v130, v7
	v_add_f32_e32 v7, 1.0, v11
	v_and_b32_e32 v11, 0xffff0000, v215
	v_rcp_f32_e32 v131, v7
	v_add_f32_e32 v7, 1.0, v132
	v_mul_f32_e32 v11, 0xbfb8aa3b, v11
	v_lshlrev_b32_e32 v132, 16, v216
	v_exp_f32_e32 v11, v11
	v_mul_f32_e32 v132, 0xbfb8aa3b, v132
	v_exp_f32_e32 v134, v132
	v_rcp_f32_e32 v132, v7
	v_add_f32_e32 v7, 1.0, v11
	v_rcp_f32_e32 v133, v7
	v_add_f32_e32 v7, 1.0, v134
	v_rcp_f32_e32 v134, v7
	v_and_b32_e32 v7, 0xffff0000, v216
	v_lshlrev_b32_e32 v11, 16, v217
	v_mul_f32_e32 v7, 0xbfb8aa3b, v7
	v_mul_f32_e32 v11, 0xbfb8aa3b, v11
	v_and_b32_e32 v135, 0xffff0000, v217
	v_exp_f32_e32 v7, v7
	v_exp_f32_e32 v11, v11
	v_mul_f32_e32 v135, 0xbfb8aa3b, v135
	v_exp_f32_e32 v135, v135
	v_add_f32_e32 v7, 1.0, v7
	v_add_f32_e32 v11, 1.0, v11
	v_rcp_f32_e32 v136, v11
	v_add_f32_e32 v11, 1.0, v135
	v_rcp_f32_e32 v135, v7
	v_rcp_f32_e32 v137, v11
	v_lshlrev_b32_e32 v7, 16, v0
	v_mul_f32_e32 v7, 0xbfb8aa3b, v7
	v_exp_f32_e32 v7, v7
	v_pk_mul_f32 v[124:125], v[124:125], v[130:131]
	v_pk_mul_f32 v[120:121], v[120:121], v[134:135]
	v_pk_mul_f32 v[126:127], v[126:127], v[132:133]
	v_pk_mul_f32 v[130:131], v[122:123], v[136:137]
	v_cvt_pk_bf16_f32 v122, v124, v125
	v_cvt_pk_bf16_f32 v123, v126, v127
	v_cvt_pk_bf16_f32 v124, v120, v121
	v_lshlrev_b64 v[120:121], 12, v[168:169]
	v_lshl_add_u64 v[120:121], s[6:7], 0, v[120:121]
	v_lshl_add_u64 v[120:121], v[120:121], 0, v[4:5]
	v_add_f32_e32 v7, 1.0, v7
	v_cvt_pk_bf16_f32 v125, v130, v131
	global_store_dwordx4 v[120:121], v[122:125], off
	v_and_b32_e32 v0, 0xffff0000, v0
	v_mul_f32_e32 v0, 0xbfb8aa3b, v0
	v_rcp_f32_e32 v122, v7
	v_lshlrev_b32_e32 v7, 16, v2
	v_mul_f32_e32 v7, 0xbfb8aa3b, v7
	v_exp_f32_e32 v7, v7
	v_lshlrev_b32_e32 v11, 16, v1
	v_and_b32_e32 v2, 0xffff0000, v2
	v_exp_f32_e32 v0, v0
	v_add_f32_e32 v7, 1.0, v7
	v_rcp_f32_e32 v124, v7
	v_lshlrev_b32_e32 v7, 16, v3
	v_and_b32_e32 v3, 0xffff0000, v3
	v_mul_f32_e32 v11, 0xbfb8aa3b, v11
	v_and_b32_e32 v1, 0xffff0000, v1
	v_mul_f32_e32 v2, 0xbfb8aa3b, v2
	v_mul_f32_e32 v7, 0xbfb8aa3b, v7
	v_mul_f32_e32 v3, 0xbfb8aa3b, v3
	v_exp_f32_e32 v11, v11
	v_mul_f32_e32 v1, 0xbfb8aa3b, v1
	v_exp_f32_e32 v2, v2
	v_exp_f32_e32 v7, v7
	v_exp_f32_e32 v3, v3
	v_exp_f32_e32 v1, v1
	v_add_f32_e32 v0, 1.0, v0
	v_rcp_f32_e32 v123, v0
	v_add_f32_e32 v0, 1.0, v11
	v_add_f32_e32 v11, 1.0, v2
	v_add_f32_e32 v2, 1.0, v7
	v_add_f32_e32 v3, 1.0, v3
	v_add_f32_e32 v1, 1.0, v1
	v_rcp_f32_e32 v2, v2
	v_rcp_f32_e32 v3, v3
	v_rcp_f32_e32 v125, v11
	v_rcp_f32_e32 v0, v0
	v_rcp_f32_e32 v1, v1
	v_pk_mul_f32 v[114:115], v[114:115], v[2:3]
	v_pk_mul_f32 v[2:3], v[112:113], v[124:125]
	v_lshlrev_b64 v[112:113], 12, v[162:163]
	v_pk_mul_f32 v[118:119], v[118:119], v[0:1]
	v_pk_mul_f32 v[0:1], v[116:117], v[122:123]
	v_lshl_add_u64 v[112:113], s[6:7], 0, v[112:113]
	v_cvt_pk_bf16_f32 v0, v0, v1
	v_lshl_add_u64 v[112:113], v[112:113], 0, v[4:5]
	v_cvt_pk_bf16_f32 v1, v118, v119
	v_cvt_pk_bf16_f32 v2, v2, v3
	v_cvt_pk_bf16_f32 v3, v114, v115
	global_store_dwordx4 v[112:113], v[0:3], off
	s_nop 1
	v_or_b32_e32 v0, 0x80, v10
	v_ashrrev_i32_e32 v1, 31, v0
	v_lshlrev_b64 v[10:11], 1, v[0:1]
	v_lshl_add_u64 v[0:1], v[12:13], 0, v[10:11]
	global_load_dwordx4 v[114:117], v[0:1], off
	v_lshl_add_u64 v[0:1], v[14:15], 0, v[10:11]
	global_load_dwordx4 v[12:15], v[0:1], off
	v_lshl_add_u64 v[0:1], v[166:167], 0, v[10:11]
	s_waitcnt vmcnt(0)
	v_lshlrev_b32_e32 v2, 16, v114
	v_mul_f32_e32 v2, 0xbfb8aa3b, v2
	v_exp_f32_e32 v7, v2
	v_lshl_add_u64 v[2:3], v[164:165], 0, v[10:11]
	global_load_dwordx4 v[122:125], v[0:1], off
	s_nop 0
	global_load_dwordx4 v[0:3], v[2:3], off
	v_and_b32_e32 v114, 0xffff0000, v114
	v_mul_f32_e32 v114, 0xbfb8aa3b, v114
	v_exp_f32_e32 v114, v114
	v_lshlrev_b32_e32 v118, 16, v115
	v_add_f32_e32 v7, 1.0, v7
	v_mul_f32_e32 v118, 0xbfb8aa3b, v118
	v_exp_f32_e32 v126, v118
	v_rcp_f32_e32 v118, v7
	v_add_f32_e32 v7, 1.0, v114
	v_and_b32_e32 v114, 0xffff0000, v115
	v_mul_f32_e32 v114, 0xbfb8aa3b, v114
	v_exp_f32_e32 v115, v114
	v_lshlrev_b32_e32 v114, 16, v116
	v_mul_f32_e32 v114, 0xbfb8aa3b, v114
	v_rcp_f32_e32 v119, v7
	v_add_f32_e32 v7, 1.0, v126
	v_exp_f32_e32 v126, v114
	v_rcp_f32_e32 v114, v7
	v_add_f32_e32 v7, 1.0, v115
	v_rcp_f32_e32 v115, v7
	v_add_f32_e32 v7, 1.0, v126
	v_rcp_f32_e32 v126, v7
	v_and_b32_e32 v7, 0xffff0000, v116
	v_lshlrev_b32_e32 v116, 16, v117
	v_and_b32_e32 v117, 0xffff0000, v117
	v_mul_f32_e32 v7, 0xbfb8aa3b, v7
	v_mul_f32_e32 v116, 0xbfb8aa3b, v116
	v_mul_f32_e32 v117, 0xbfb8aa3b, v117
	v_exp_f32_e32 v7, v7
	v_exp_f32_e32 v116, v116
	v_exp_f32_e32 v117, v117
	v_pk_mul_f32 v[110:111], v[110:111], v[114:115]
	v_add_f32_e32 v7, 1.0, v7
	v_add_f32_e32 v116, 1.0, v116
	v_add_f32_e32 v117, 1.0, v117
	v_rcp_f32_e32 v116, v116
	v_rcp_f32_e32 v117, v117
	v_rcp_f32_e32 v127, v7
	v_lshlrev_b32_e32 v7, 16, v12
	v_mul_f32_e32 v7, 0xbfb8aa3b, v7
	v_and_b32_e32 v12, 0xffff0000, v12
	v_exp_f32_e32 v7, v7
	v_mul_f32_e32 v12, 0xbfb8aa3b, v12
	v_exp_f32_e32 v12, v12
	v_pk_mul_f32 v[108:109], v[108:109], v[118:119]
	v_pk_mul_f32 v[114:115], v[106:107], v[116:117]
	v_pk_mul_f32 v[106:107], v[104:105], v[126:127]
	v_cvt_pk_bf16_f32 v104, v108, v109
	v_cvt_pk_bf16_f32 v105, v110, v111
	v_add_f32_e32 v7, 1.0, v7
	v_cvt_pk_bf16_f32 v106, v106, v107
	v_cvt_pk_bf16_f32 v107, v114, v115
	global_store_dwordx4 v[160:161], v[104:107], off offset:256
	s_nop 1
	v_lshlrev_b32_e32 v104, 16, v13
	v_mul_f32_e32 v104, 0xbfb8aa3b, v104
	v_exp_f32_e32 v106, v104
	v_rcp_f32_e32 v104, v7
	v_add_f32_e32 v7, 1.0, v12
	v_and_b32_e32 v12, 0xffff0000, v13
	v_mul_f32_e32 v12, 0xbfb8aa3b, v12
	v_exp_f32_e32 v13, v12
	v_lshlrev_b32_e32 v12, 16, v14
	v_mul_f32_e32 v12, 0xbfb8aa3b, v12
	v_rcp_f32_e32 v105, v7
	v_add_f32_e32 v7, 1.0, v106
	v_exp_f32_e32 v106, v12
	v_rcp_f32_e32 v12, v7
	v_add_f32_e32 v7, 1.0, v13
	v_rcp_f32_e32 v13, v7
	v_add_f32_e32 v7, 1.0, v106
	v_rcp_f32_e32 v106, v7
	v_and_b32_e32 v7, 0xffff0000, v14
	v_lshlrev_b32_e32 v14, 16, v15
	v_and_b32_e32 v15, 0xffff0000, v15
	v_mul_f32_e32 v7, 0xbfb8aa3b, v7
	v_mul_f32_e32 v14, 0xbfb8aa3b, v14
	v_mul_f32_e32 v15, 0xbfb8aa3b, v15
	v_exp_f32_e32 v7, v7
	v_exp_f32_e32 v14, v14
	v_exp_f32_e32 v15, v15
	v_pk_mul_f32 v[102:103], v[102:103], v[12:13]
	v_add_f32_e32 v7, 1.0, v7
	v_add_f32_e32 v14, 1.0, v14
	v_add_f32_e32 v15, 1.0, v15
	v_rcp_f32_e32 v14, v14
	v_rcp_f32_e32 v15, v15
	v_rcp_f32_e32 v107, v7
	v_pk_mul_f32 v[12:13], v[100:101], v[104:105]
	s_waitcnt vmcnt(0)
	v_lshlrev_b32_e32 v7, 16, v122
	v_pk_mul_f32 v[98:99], v[98:99], v[14:15]
	v_pk_mul_f32 v[14:15], v[96:97], v[106:107]
	v_cvt_pk_bf16_f32 v12, v12, v13
	v_cvt_pk_bf16_f32 v13, v102, v103
	v_mul_f32_e32 v7, 0xbfb8aa3b, v7
	v_cvt_pk_bf16_f32 v14, v14, v15
	v_cvt_pk_bf16_f32 v15, v98, v99
	global_store_dwordx4 v[128:129], v[12:15], off offset:256
	v_exp_f32_e32 v7, v7
	v_lshlrev_b32_e32 v97, 16, v125
	v_and_b32_e32 v12, 0xffff0000, v122
	v_mul_f32_e32 v12, 0xbfb8aa3b, v12
	v_exp_f32_e32 v13, v12
	v_lshlrev_b32_e32 v12, 16, v123
	v_mul_f32_e32 v12, 0xbfb8aa3b, v12
	v_exp_f32_e32 v14, v12
	v_add_f32_e32 v7, 1.0, v7
	v_rcp_f32_e32 v12, v7
	v_add_f32_e32 v7, 1.0, v13
	v_rcp_f32_e32 v13, v7
	v_add_f32_e32 v7, 1.0, v14
	v_and_b32_e32 v14, 0xffff0000, v123
	v_mul_f32_e32 v14, 0xbfb8aa3b, v14
	v_exp_f32_e32 v15, v14
	v_lshlrev_b32_e32 v14, 16, v124
	v_mul_f32_e32 v14, 0xbfb8aa3b, v14
	v_exp_f32_e32 v96, v14
	v_rcp_f32_e32 v14, v7
	v_add_f32_e32 v7, 1.0, v15
	v_rcp_f32_e32 v15, v7
	v_add_f32_e32 v7, 1.0, v96
	v_rcp_f32_e32 v96, v7
	v_and_b32_e32 v7, 0xffff0000, v124
	v_mul_f32_e32 v97, 0xbfb8aa3b, v97
	v_and_b32_e32 v98, 0xffff0000, v125
	v_mul_f32_e32 v7, 0xbfb8aa3b, v7
	v_exp_f32_e32 v97, v97
	v_mul_f32_e32 v98, 0xbfb8aa3b, v98
	v_exp_f32_e32 v7, v7
	v_exp_f32_e32 v99, v98
	v_add_f32_e32 v97, 1.0, v97
	v_rcp_f32_e32 v98, v97
	v_add_f32_e32 v7, 1.0, v7
	v_add_f32_e32 v97, 1.0, v99
	v_rcp_f32_e32 v99, v97
	v_rcp_f32_e32 v97, v7
	v_lshlrev_b32_e32 v7, 16, v0
	v_mul_f32_e32 v7, 0xbfb8aa3b, v7
	v_exp_f32_e32 v7, v7
	v_pk_mul_f32 v[12:13], v[92:93], v[12:13]
	v_pk_mul_f32 v[14:15], v[94:95], v[14:15]
	v_cvt_pk_bf16_f32 v12, v12, v13
	v_pk_mul_f32 v[90:91], v[90:91], v[98:99]
	v_pk_mul_f32 v[88:89], v[88:89], v[96:97]
	v_cvt_pk_bf16_f32 v13, v14, v15
	v_add_f32_e32 v7, 1.0, v7
	v_cvt_pk_bf16_f32 v14, v88, v89
	v_cvt_pk_bf16_f32 v15, v90, v91
	global_store_dwordx4 v[120:121], v[12:15], off offset:256
	v_and_b32_e32 v0, 0xffff0000, v0
	v_mul_f32_e32 v0, 0xbfb8aa3b, v0
	v_lshlrev_b32_e32 v12, 16, v1
	v_mul_f32_e32 v12, 0xbfb8aa3b, v12
	v_exp_f32_e32 v14, v12
	v_rcp_f32_e32 v12, v7
	v_lshlrev_b32_e32 v7, 16, v2
	v_mul_f32_e32 v7, 0xbfb8aa3b, v7
	v_exp_f32_e32 v0, v0
	v_exp_f32_e32 v7, v7
	v_and_b32_e32 v1, 0xffff0000, v1
	v_mul_f32_e32 v1, 0xbfb8aa3b, v1
	v_add_f32_e32 v0, 1.0, v0
	v_add_f32_e32 v7, 1.0, v7
	v_rcp_f32_e32 v13, v0
	v_add_f32_e32 v0, 1.0, v14
	v_rcp_f32_e32 v14, v7
	v_and_b32_e32 v2, 0xffff0000, v2
	v_lshlrev_b32_e32 v7, 16, v3
	v_and_b32_e32 v3, 0xffff0000, v3
	v_exp_f32_e32 v1, v1
	v_mul_f32_e32 v2, 0xbfb8aa3b, v2
	v_mul_f32_e32 v7, 0xbfb8aa3b, v7
	v_mul_f32_e32 v3, 0xbfb8aa3b, v3
	v_exp_f32_e32 v2, v2
	v_exp_f32_e32 v7, v7
	v_exp_f32_e32 v3, v3
	v_add_f32_e32 v1, 1.0, v1
	v_rcp_f32_e32 v0, v0
	v_rcp_f32_e32 v1, v1
	v_add_f32_e32 v15, 1.0, v2
	v_add_f32_e32 v2, 1.0, v7
	v_add_f32_e32 v3, 1.0, v3
	v_rcp_f32_e32 v2, v2
	v_rcp_f32_e32 v3, v3
	v_rcp_f32_e32 v15, v15
	v_pk_mul_f32 v[86:87], v[86:87], v[0:1]
	v_pk_mul_f32 v[0:1], v[84:85], v[12:13]
	v_pk_mul_f32 v[12:13], v[82:83], v[2:3]
	v_pk_mul_f32 v[2:3], v[80:81], v[14:15]
	v_cvt_pk_bf16_f32 v0, v0, v1
	v_cvt_pk_bf16_f32 v1, v86, v87
	v_add_u32_e32 v98, 0x80, v6
	v_cvt_pk_bf16_f32 v2, v2, v3
	v_cvt_pk_bf16_f32 v3, v12, v13
	global_store_dwordx4 v[112:113], v[0:3], off offset:256
	v_add_u32_e32 v100, 0x90, v6
	v_add_u32_e32 v82, 0xb0, v6
	v_mad_i64_i32 v[0:1], s[30:31], v98, s59, v[8:9]
	v_lshl_add_u64 v[12:13], v[0:1], 0, s[16:17]
	v_lshl_add_u64 v[0:1], v[12:13], 0, v[4:5]
	global_load_dwordx4 v[86:89], v[0:1], off
	v_mad_i64_i32 v[0:1], s[30:31], v100, s59, v[8:9]
	v_lshl_add_u64 v[14:15], v[0:1], 0, s[16:17]
	v_lshl_add_u64 v[0:1], v[14:15], 0, v[4:5]
	global_load_dwordx4 v[90:93], v[0:1], off
	v_add_u32_e32 v84, 0xa0, v6
	v_mad_i64_i32 v[2:3], s[30:31], v82, s59, v[8:9]
	v_mad_i64_i32 v[0:1], s[30:31], v84, s59, v[8:9]
	v_lshl_add_u64 v[6:7], v[2:3], 0, s[16:17]
	v_lshl_add_u64 v[80:81], v[0:1], 0, s[16:17]
	v_lshl_add_u64 v[0:1], v[80:81], 0, v[4:5]
	v_ashrrev_i32_e32 v99, 31, v98
	v_ashrrev_i32_e32 v101, 31, v100
	v_ashrrev_i32_e32 v85, 31, v84
	v_ashrrev_i32_e32 v83, 31, v82
	s_mov_b64 s[30:31], s[24:25]
	s_waitcnt vmcnt(0)
	v_lshlrev_b32_e32 v2, 16, v86
	v_mul_f32_e32 v2, 0xbfb8aa3b, v2
	v_exp_f32_e32 v8, v2
	v_lshl_add_u64 v[2:3], v[6:7], 0, v[4:5]
	global_load_dwordx4 v[94:97], v[0:1], off
	s_nop 0
	global_load_dwordx4 v[0:3], v[2:3], off
	v_and_b32_e32 v9, 0xffff0000, v86
	v_lshlrev_b32_e32 v102, 16, v88
	v_and_b32_e32 v88, 0xffff0000, v88
	v_lshlrev_b32_e32 v103, 16, v89
	v_and_b32_e32 v89, 0xffff0000, v89
	v_mul_f32_e32 v9, 0xbfb8aa3b, v9
	v_lshlrev_b32_e32 v86, 16, v87
	v_and_b32_e32 v87, 0xffff0000, v87
	v_mul_f32_e32 v102, 0xbfb8aa3b, v102
	v_mul_f32_e32 v88, 0xbfb8aa3b, v88
	v_mul_f32_e32 v103, 0xbfb8aa3b, v103
	v_mul_f32_e32 v89, 0xbfb8aa3b, v89
	v_exp_f32_e32 v9, v9
	v_mul_f32_e32 v86, 0xbfb8aa3b, v86
	v_mul_f32_e32 v87, 0xbfb8aa3b, v87
	v_exp_f32_e32 v102, v102
	v_exp_f32_e32 v88, v88
	v_exp_f32_e32 v103, v103
	v_exp_f32_e32 v89, v89
	v_exp_f32_e32 v86, v86
	v_exp_f32_e32 v87, v87
	v_add_f32_e32 v8, 1.0, v8
	v_add_f32_e32 v9, 1.0, v9
	v_add_f32_e32 v102, 1.0, v102
	v_add_f32_e32 v104, 1.0, v88
	v_add_f32_e32 v88, 1.0, v103
	v_add_f32_e32 v89, 1.0, v89
	v_rcp_f32_e32 v8, v8
	v_rcp_f32_e32 v9, v9
	v_add_f32_e32 v86, 1.0, v86
	v_add_f32_e32 v87, 1.0, v87
	v_rcp_f32_e32 v102, v102
	v_rcp_f32_e32 v88, v88
	v_rcp_f32_e32 v89, v89
	v_rcp_f32_e32 v103, v104
	v_rcp_f32_e32 v86, v86
	v_rcp_f32_e32 v87, v87
	v_pk_mul_f32 v[8:9], v[76:77], v[8:9]
	v_pk_mul_f32 v[76:77], v[74:75], v[88:89]
	v_pk_mul_f32 v[74:75], v[72:73], v[102:103]
	v_pk_mul_f32 v[78:79], v[78:79], v[86:87]
	v_cvt_pk_bf16_f32 v72, v8, v9
	v_lshlrev_b64 v[8:9], 12, v[98:99]
	v_cvt_pk_bf16_f32 v73, v78, v79
	v_cvt_pk_bf16_f32 v74, v74, v75
	v_cvt_pk_bf16_f32 v75, v76, v77
	v_lshlrev_b32_e32 v76, 16, v90
	v_mul_f32_e32 v76, 0xbfb8aa3b, v76
	v_lshl_add_u64 v[8:9], s[6:7], 0, v[8:9]
	v_exp_f32_e32 v76, v76
	v_lshl_add_u64 v[8:9], v[8:9], 0, v[4:5]
	global_store_dwordx4 v[8:9], v[72:75], off
	v_lshlrev_b32_e32 v78, 16, v93
	v_and_b32_e32 v79, 0xffff0000, v93
	v_lshlrev_b32_e32 v74, 16, v91
	v_and_b32_e32 v75, 0xffff0000, v91
	v_and_b32_e32 v73, 0xffff0000, v90
	v_mul_f32_e32 v74, 0xbfb8aa3b, v74
	v_mul_f32_e32 v75, 0xbfb8aa3b, v75
	v_mul_f32_e32 v73, 0xbfb8aa3b, v73
	v_exp_f32_e32 v74, v74
	v_exp_f32_e32 v75, v75
	v_mul_f32_e32 v78, 0xbfb8aa3b, v78
	v_mul_f32_e32 v79, 0xbfb8aa3b, v79
	v_add_f32_e32 v72, 1.0, v76
	v_exp_f32_e32 v73, v73
	v_lshlrev_b32_e32 v76, 16, v92
	v_and_b32_e32 v77, 0xffff0000, v92
	v_exp_f32_e32 v78, v78
	v_exp_f32_e32 v79, v79
	v_mul_f32_e32 v76, 0xbfb8aa3b, v76
	v_mul_f32_e32 v77, 0xbfb8aa3b, v77
	v_exp_f32_e32 v76, v76
	v_exp_f32_e32 v77, v77
	v_add_f32_e32 v74, 1.0, v74
	v_add_f32_e32 v75, 1.0, v75
	v_add_f32_e32 v73, 1.0, v73
	v_rcp_f32_e32 v74, v74
	v_rcp_f32_e32 v75, v75
	v_add_f32_e32 v78, 1.0, v78
	v_add_f32_e32 v79, 1.0, v79
	v_rcp_f32_e32 v72, v72
	v_rcp_f32_e32 v73, v73
	v_rcp_f32_e32 v78, v78
	v_rcp_f32_e32 v79, v79
	v_add_f32_e32 v76, 1.0, v76
	v_add_f32_e32 v77, 1.0, v77
	v_rcp_f32_e32 v76, v76
	v_rcp_f32_e32 v77, v77
	v_pk_mul_f32 v[70:71], v[70:71], v[74:75]
	v_pk_mul_f32 v[68:69], v[68:69], v[72:73]
	v_pk_mul_f32 v[72:73], v[66:67], v[78:79]
	v_cvt_pk_bf16_f32 v66, v68, v69
	v_cvt_pk_bf16_f32 v67, v70, v71
	s_waitcnt vmcnt(0)
	v_lshlrev_b32_e32 v70, 16, v94
	v_mul_f32_e32 v70, 0xbfb8aa3b, v70
	v_pk_mul_f32 v[64:65], v[64:65], v[76:77]
	v_exp_f32_e32 v70, v70
	v_cvt_pk_bf16_f32 v68, v64, v65
	v_lshlrev_b64 v[64:65], 12, v[100:101]
	v_lshl_add_u64 v[64:65], s[6:7], 0, v[64:65]
	v_lshl_add_u64 v[64:65], v[64:65], 0, v[4:5]
	v_cvt_pk_bf16_f32 v69, v72, v73
	global_store_dwordx4 v[64:65], v[66:69], off
	v_and_b32_e32 v71, 0xffff0000, v96
	v_mul_f32_e32 v71, 0xbfb8aa3b, v71
	v_add_f32_e32 v66, 1.0, v70
	v_and_b32_e32 v67, 0xffff0000, v94
	v_lshlrev_b32_e32 v70, 16, v96
	v_mul_f32_e32 v67, 0xbfb8aa3b, v67
	v_lshlrev_b32_e32 v68, 16, v95
	v_and_b32_e32 v69, 0xffff0000, v95
	v_mul_f32_e32 v70, 0xbfb8aa3b, v70
	v_lshlrev_b32_e32 v72, 16, v97
	v_and_b32_e32 v73, 0xffff0000, v97
	v_exp_f32_e32 v67, v67
	v_mul_f32_e32 v68, 0xbfb8aa3b, v68
	v_mul_f32_e32 v69, 0xbfb8aa3b, v69
	v_exp_f32_e32 v70, v70
	v_exp_f32_e32 v71, v71
	v_mul_f32_e32 v72, 0xbfb8aa3b, v72
	v_mul_f32_e32 v73, 0xbfb8aa3b, v73
	v_exp_f32_e32 v68, v68
	v_exp_f32_e32 v69, v69
	v_exp_f32_e32 v72, v72
	v_exp_f32_e32 v73, v73
	v_add_f32_e32 v67, 1.0, v67
	v_add_f32_e32 v70, 1.0, v70
	v_add_f32_e32 v71, 1.0, v71
	v_rcp_f32_e32 v66, v66
	v_rcp_f32_e32 v67, v67
	v_add_f32_e32 v68, 1.0, v68
	v_add_f32_e32 v69, 1.0, v69
	v_rcp_f32_e32 v70, v70
	v_add_f32_e32 v72, 1.0, v72
	v_add_f32_e32 v73, 1.0, v73
	v_rcp_f32_e32 v71, v71
	v_rcp_f32_e32 v68, v68
	v_rcp_f32_e32 v69, v69
	v_rcp_f32_e32 v72, v72
	v_rcp_f32_e32 v73, v73
	v_pk_mul_f32 v[60:61], v[60:61], v[66:67]
	v_pk_mul_f32 v[56:57], v[56:57], v[70:71]
	v_pk_mul_f32 v[62:63], v[62:63], v[68:69]
	v_pk_mul_f32 v[66:67], v[58:59], v[72:73]
	v_cvt_pk_bf16_f32 v58, v60, v61
	v_cvt_pk_bf16_f32 v59, v62, v63
	v_cvt_pk_bf16_f32 v60, v56, v57
	v_lshlrev_b64 v[56:57], 12, v[84:85]
	v_lshl_add_u64 v[56:57], s[6:7], 0, v[56:57]
	v_lshlrev_b32_e32 v62, 16, v0
	v_lshl_add_u64 v[56:57], v[56:57], 0, v[4:5]
	v_and_b32_e32 v0, 0xffff0000, v0
	v_cvt_pk_bf16_f32 v61, v66, v67
	global_store_dwordx4 v[56:57], v[58:61], off
	v_mul_f32_e32 v0, 0xbfb8aa3b, v0
	v_exp_f32_e32 v0, v0
	v_lshlrev_b32_e32 v59, 16, v1
	v_mul_f32_e32 v59, 0xbfb8aa3b, v59
	v_exp_f32_e32 v60, v59
	v_add_f32_e32 v0, 1.0, v0
	v_rcp_f32_e32 v59, v0
	v_lshlrev_b32_e32 v61, 16, v3
	v_add_f32_e32 v0, 1.0, v60
	v_lshlrev_b32_e32 v60, 16, v2
	v_and_b32_e32 v2, 0xffff0000, v2
	v_and_b32_e32 v3, 0xffff0000, v3
	v_mul_f32_e32 v62, 0xbfb8aa3b, v62
	v_mul_f32_e32 v60, 0xbfb8aa3b, v60
	v_mul_f32_e32 v2, 0xbfb8aa3b, v2
	v_mul_f32_e32 v61, 0xbfb8aa3b, v61
	v_mul_f32_e32 v3, 0xbfb8aa3b, v3
	v_exp_f32_e32 v62, v62
	v_and_b32_e32 v1, 0xffff0000, v1
	v_exp_f32_e32 v60, v60
	v_exp_f32_e32 v2, v2
	v_exp_f32_e32 v61, v61
	v_exp_f32_e32 v3, v3
	v_mul_f32_e32 v1, 0xbfb8aa3b, v1
	v_exp_f32_e32 v1, v1
	v_add_f32_e32 v58, 1.0, v62
	v_add_f32_e32 v60, 1.0, v60
	v_add_f32_e32 v62, 1.0, v2
	v_add_f32_e32 v2, 1.0, v61
	v_add_f32_e32 v3, 1.0, v3
	v_rcp_f32_e32 v60, v60
	v_rcp_f32_e32 v2, v2
	v_rcp_f32_e32 v3, v3
	v_rcp_f32_e32 v61, v62
	v_add_f32_e32 v1, 1.0, v1
	v_rcp_f32_e32 v58, v58
	v_rcp_f32_e32 v0, v0
	v_rcp_f32_e32 v1, v1
	v_pk_mul_f32 v[50:51], v[50:51], v[2:3]
	v_pk_mul_f32 v[2:3], v[48:49], v[60:61]
	v_lshlrev_b64 v[48:49], 12, v[82:83]
	v_lshl_add_u64 v[48:49], s[6:7], 0, v[48:49]
	v_pk_mul_f32 v[54:55], v[54:55], v[0:1]
	v_pk_mul_f32 v[0:1], v[52:53], v[58:59]
	v_lshl_add_u64 v[4:5], v[48:49], 0, v[4:5]
	v_cvt_pk_bf16_f32 v0, v0, v1
	v_cvt_pk_bf16_f32 v1, v54, v55
	v_cvt_pk_bf16_f32 v2, v2, v3
	v_cvt_pk_bf16_f32 v3, v50, v51
	global_store_dwordx4 v[4:5], v[0:3], off
	s_nop 1
	v_lshl_add_u64 v[0:1], v[12:13], 0, v[10:11]
	global_load_dwordx4 v[48:51], v[0:1], off
	v_lshl_add_u64 v[0:1], v[14:15], 0, v[10:11]
	global_load_dwordx4 v[12:15], v[0:1], off
	v_lshl_add_u64 v[0:1], v[80:81], 0, v[10:11]
	s_waitcnt vmcnt(0)
	v_lshlrev_b32_e32 v2, 16, v48
	v_mul_f32_e32 v2, 0xbfb8aa3b, v2
	v_exp_f32_e32 v58, v2
	v_lshl_add_u64 v[2:3], v[6:7], 0, v[10:11]
	global_load_dwordx4 v[52:55], v[0:1], off
	s_nop 0
	global_load_dwordx4 v[0:3], v[2:3], off
	v_and_b32_e32 v7, 0xffff0000, v48
	v_lshlrev_b32_e32 v10, 16, v49
	v_and_b32_e32 v11, 0xffff0000, v49
	v_lshlrev_b32_e32 v48, 16, v50
	v_and_b32_e32 v49, 0xffff0000, v50
	v_lshlrev_b32_e32 v50, 16, v51
	v_and_b32_e32 v51, 0xffff0000, v51
	v_mul_f32_e32 v7, 0xbfb8aa3b, v7
	v_mul_f32_e32 v48, 0xbfb8aa3b, v48
	v_mul_f32_e32 v49, 0xbfb8aa3b, v49
	v_mul_f32_e32 v50, 0xbfb8aa3b, v50
	v_mul_f32_e32 v51, 0xbfb8aa3b, v51
	v_exp_f32_e32 v7, v7
	v_mul_f32_e32 v10, 0xbfb8aa3b, v10
	v_mul_f32_e32 v11, 0xbfb8aa3b, v11
	v_exp_f32_e32 v48, v48
	v_exp_f32_e32 v49, v49
	v_exp_f32_e32 v50, v50
	v_exp_f32_e32 v51, v51
	v_exp_f32_e32 v10, v10
	v_exp_f32_e32 v11, v11
	v_add_f32_e32 v6, 1.0, v58
	v_add_f32_e32 v7, 1.0, v7
	v_add_f32_e32 v48, 1.0, v48
	v_add_f32_e32 v49, 1.0, v49
	v_add_f32_e32 v50, 1.0, v50
	v_add_f32_e32 v51, 1.0, v51
	v_rcp_f32_e32 v6, v6
	v_rcp_f32_e32 v7, v7
	v_add_f32_e32 v10, 1.0, v10
	v_add_f32_e32 v11, 1.0, v11
	v_rcp_f32_e32 v48, v48
	v_rcp_f32_e32 v50, v50
	v_rcp_f32_e32 v51, v51
	v_rcp_f32_e32 v49, v49
	v_rcp_f32_e32 v10, v10
	v_rcp_f32_e32 v11, v11
	v_pk_mul_f32 v[6:7], v[44:45], v[6:7]
	v_pk_mul_f32 v[44:45], v[42:43], v[50:51]
	v_pk_mul_f32 v[42:43], v[40:41], v[48:49]
	v_pk_mul_f32 v[10:11], v[46:47], v[10:11]
	v_cvt_pk_bf16_f32 v40, v6, v7
	v_lshlrev_b32_e32 v6, 16, v12
	v_cvt_pk_bf16_f32 v41, v10, v11
	v_cvt_pk_bf16_f32 v42, v42, v43
	v_cvt_pk_bf16_f32 v43, v44, v45
	global_store_dwordx4 v[8:9], v[40:43], off offset:256
	v_and_b32_e32 v7, 0xffff0000, v12
	v_lshlrev_b32_e32 v8, 16, v13
	v_and_b32_e32 v9, 0xffff0000, v13
	v_mul_f32_e32 v6, 0xbfb8aa3b, v6
	v_mul_f32_e32 v7, 0xbfb8aa3b, v7
	v_mul_f32_e32 v8, 0xbfb8aa3b, v8
	v_mul_f32_e32 v9, 0xbfb8aa3b, v9
	v_exp_f32_e32 v6, v6
	v_exp_f32_e32 v7, v7
	v_exp_f32_e32 v8, v8
	v_exp_f32_e32 v9, v9
	v_lshlrev_b32_e32 v10, 16, v14
	v_and_b32_e32 v11, 0xffff0000, v14
	v_lshlrev_b32_e32 v12, 16, v15
	v_and_b32_e32 v13, 0xffff0000, v15
	v_mul_f32_e32 v10, 0xbfb8aa3b, v10
	v_mul_f32_e32 v11, 0xbfb8aa3b, v11
	v_mul_f32_e32 v12, 0xbfb8aa3b, v12
	v_mul_f32_e32 v13, 0xbfb8aa3b, v13
	v_exp_f32_e32 v10, v10
	v_exp_f32_e32 v11, v11
	v_exp_f32_e32 v12, v12
	v_exp_f32_e32 v13, v13
	v_add_f32_e32 v6, 1.0, v6
	v_add_f32_e32 v7, 1.0, v7
	v_add_f32_e32 v8, 1.0, v8
	v_add_f32_e32 v9, 1.0, v9
	v_rcp_f32_e32 v6, v6
	v_rcp_f32_e32 v7, v7
	v_rcp_f32_e32 v8, v8
	v_rcp_f32_e32 v9, v9
	v_add_f32_e32 v10, 1.0, v10
	v_add_f32_e32 v11, 1.0, v11
	v_add_f32_e32 v12, 1.0, v12
	v_add_f32_e32 v13, 1.0, v13
	v_rcp_f32_e32 v10, v10
	v_rcp_f32_e32 v12, v12
	v_rcp_f32_e32 v13, v13
	v_rcp_f32_e32 v11, v11
	v_pk_mul_f32 v[8:9], v[38:39], v[8:9]
	v_pk_mul_f32 v[6:7], v[36:37], v[6:7]
	v_pk_mul_f32 v[12:13], v[34:35], v[12:13]
	v_cvt_pk_bf16_f32 v6, v6, v7
	v_cvt_pk_bf16_f32 v7, v8, v9
	s_waitcnt vmcnt(0)
	v_lshlrev_b32_e32 v8, 16, v52
	v_mul_f32_e32 v8, 0xbfb8aa3b, v8
	v_pk_mul_f32 v[10:11], v[32:33], v[10:11]
	v_exp_f32_e32 v14, v8
	v_cvt_pk_bf16_f32 v8, v10, v11
	v_cvt_pk_bf16_f32 v9, v12, v13
	global_store_dwordx4 v[64:65], v[6:9], off offset:256
	v_lshlrev_b32_e32 v10, 16, v54
	v_and_b32_e32 v11, 0xffff0000, v54
	v_and_b32_e32 v7, 0xffff0000, v52
	v_lshlrev_b32_e32 v8, 16, v53
	v_and_b32_e32 v9, 0xffff0000, v53
	v_mul_f32_e32 v7, 0xbfb8aa3b, v7
	v_mul_f32_e32 v8, 0xbfb8aa3b, v8
	v_mul_f32_e32 v9, 0xbfb8aa3b, v9
	v_exp_f32_e32 v7, v7
	v_exp_f32_e32 v8, v8
	v_exp_f32_e32 v9, v9
	v_lshlrev_b32_e32 v12, 16, v55
	v_and_b32_e32 v13, 0xffff0000, v55
	v_mul_f32_e32 v10, 0xbfb8aa3b, v10
	v_mul_f32_e32 v11, 0xbfb8aa3b, v11
	v_mul_f32_e32 v12, 0xbfb8aa3b, v12
	v_mul_f32_e32 v13, 0xbfb8aa3b, v13
	v_exp_f32_e32 v10, v10
	v_exp_f32_e32 v11, v11
	v_exp_f32_e32 v12, v12
	v_exp_f32_e32 v13, v13
	v_add_f32_e32 v6, 1.0, v14
	v_add_f32_e32 v7, 1.0, v7
	v_add_f32_e32 v8, 1.0, v8
	v_add_f32_e32 v9, 1.0, v9
	v_rcp_f32_e32 v6, v6
	v_rcp_f32_e32 v7, v7
	v_rcp_f32_e32 v8, v8
	v_rcp_f32_e32 v9, v9
	v_add_f32_e32 v10, 1.0, v10
	v_add_f32_e32 v11, 1.0, v11
	v_add_f32_e32 v12, 1.0, v12
	v_add_f32_e32 v13, 1.0, v13
	v_rcp_f32_e32 v10, v10
	v_rcp_f32_e32 v12, v12
	v_rcp_f32_e32 v13, v13
	v_rcp_f32_e32 v11, v11
	v_pk_mul_f32 v[8:9], v[30:31], v[8:9]
	v_pk_mul_f32 v[6:7], v[28:29], v[6:7]
	v_pk_mul_f32 v[12:13], v[26:27], v[12:13]
	v_cvt_pk_bf16_f32 v6, v6, v7
	v_cvt_pk_bf16_f32 v7, v8, v9
	v_lshlrev_b32_e32 v8, 16, v0
	v_mul_f32_e32 v8, 0xbfb8aa3b, v8
	v_and_b32_e32 v0, 0xffff0000, v0
	v_pk_mul_f32 v[10:11], v[24:25], v[10:11]
	v_exp_f32_e32 v14, v8
	v_cvt_pk_bf16_f32 v8, v10, v11
	v_cvt_pk_bf16_f32 v9, v12, v13
	global_store_dwordx4 v[56:57], v[6:9], off offset:256
	v_mul_f32_e32 v0, 0xbfb8aa3b, v0
	v_exp_f32_e32 v0, v0
	v_lshlrev_b32_e32 v7, 16, v1
	v_mul_f32_e32 v7, 0xbfb8aa3b, v7
	v_exp_f32_e32 v8, v7
	v_add_f32_e32 v0, 1.0, v0
	v_rcp_f32_e32 v7, v0
	v_and_b32_e32 v1, 0xffff0000, v1
	v_add_f32_e32 v0, 1.0, v8
	v_lshlrev_b32_e32 v8, 16, v2
	v_and_b32_e32 v2, 0xffff0000, v2
	v_lshlrev_b32_e32 v9, 16, v3
	v_and_b32_e32 v3, 0xffff0000, v3
	v_mul_f32_e32 v1, 0xbfb8aa3b, v1
	v_mul_f32_e32 v8, 0xbfb8aa3b, v8
	v_mul_f32_e32 v2, 0xbfb8aa3b, v2
	v_mul_f32_e32 v9, 0xbfb8aa3b, v9
	v_mul_f32_e32 v3, 0xbfb8aa3b, v3
	v_exp_f32_e32 v1, v1
	v_exp_f32_e32 v8, v8
	v_exp_f32_e32 v2, v2
	v_exp_f32_e32 v9, v9
	v_exp_f32_e32 v3, v3
	v_add_f32_e32 v6, 1.0, v14
	v_add_f32_e32 v1, 1.0, v1
	v_add_f32_e32 v8, 1.0, v8
	v_add_f32_e32 v10, 1.0, v2
	v_add_f32_e32 v2, 1.0, v9
	v_add_f32_e32 v3, 1.0, v3
	v_rcp_f32_e32 v6, v6
	v_rcp_f32_e32 v0, v0
	v_rcp_f32_e32 v1, v1
	v_rcp_f32_e32 v8, v8
	v_rcp_f32_e32 v2, v2
	v_rcp_f32_e32 v3, v3
	v_rcp_f32_e32 v9, v10
	v_pk_mul_f32 v[10:11], v[22:23], v[0:1]
	v_pk_mul_f32 v[0:1], v[20:21], v[6:7]
	v_pk_mul_f32 v[6:7], v[18:19], v[2:3]
	v_pk_mul_f32 v[2:3], v[16:17], v[8:9]
	v_cvt_pk_bf16_f32 v0, v0, v1
	v_cvt_pk_bf16_f32 v1, v10, v11
	s_nop 0
	v_cvt_pk_bf16_f32 v2, v2, v3
	v_cvt_pk_bf16_f32 v3, v6, v7
	global_store_dwordx4 v[4:5], v[0:3], off offset:256
	s_cbranch_vccz .LBB0_1018
	s_waitcnt vmcnt(0)
	s_cmpk_gt_u32 s33, 0xff
	s_cbranch_scc1 .LBB0_1029
	s_barrier
